# MoBA unit O stores: lane^1 exchange by DPP quad_perm instead of 64 serialised ds_bpermute round trips; one exec mask for the 64 stores
# baseline (speedup 1.0000x reference)
; __device__ __forceinline__ int crow(int r, int hi) { return (r & 3) + 8 * (r >> 2) + 4 * hi; }
; __device__ __forceinline__ unsigned cvtpk(float lo, float hi) { unsigned r; asm volatile("v_cvt_pk_bf16_f32 %0, %1, %2" : "=v"(r) : "v"(lo), "v"(hi)); return r; }
; __device__ __forceinline__ void moba_unit(const UnitRef& u, char* lds, int* rowtab, int* cq, float* wscr, int* idx_slot, const int pend_idx, const int wid) {
;     ...
;         if (hi == 0) li_l[r32] = l_reg; asm volatile("s_waitcnt lgkmcnt(0)" ::: "memory");
;         float rli[16];
; #pragma unroll
;         for (int r = 0; r < 16; ++r) rli[r] = __builtin_amdgcn_rcpf(li_l[crow(r, hi)]);
;         const unsigned ooff = (unsigned)((grp * 32 + 4 * hi) * OPITCH + r32) * 2u;
; #pragma unroll
;         for (int r = 0; r < 16; ++r) { const int orc = (r & 3) + 8 * (r >> 2);
; #pragma unroll
;             for (int d0 = 0; d0 < 4; ++d0) { const float v = o[d0][r] * rli[r];
;                 const float vn = __shfl_xor(v, 1);
;                 if ((r32 & 1) == 0) *(unsigned*)((char*)u.O + (size_t)(orc * OPITCH + d0 * 32) * 2 + ooff) = cvtpk(v, vn); } }
.LBB0_769:
	s_or_b64 exec, exec, s[10:11]
	s_waitcnt lgkmcnt(0)
	ds_read_b128 v[108:111], v190
	ds_read_b128 v[104:107], v190 offset:32
	ds_read_b128 v[100:103], v190 offset:64
	ds_read_b128 v[96:99], v190 offset:96
	v_lshl_add_u64 v[114:115], s[90:91], 0, v[128:129]
	s_mov_b64 s[12:13], 0x1000
	s_waitcnt lgkmcnt(0)
	v_lshl_add_u64 v[118:119], v[114:115], 0, s[12:13]
	v_rcp_f32_e32 v108, v108
	v_rcp_f32_e32 v109, v109
	v_rcp_f32_e32 v110, v110
	v_rcp_f32_e32 v111, v111
	v_rcp_f32_e32 v104, v104
	v_rcp_f32_e32 v105, v105
	v_rcp_f32_e32 v106, v106
	v_rcp_f32_e32 v107, v107
	v_rcp_f32_e32 v100, v100
	v_rcp_f32_e32 v101, v101
	v_rcp_f32_e32 v102, v102
	v_rcp_f32_e32 v103, v103
	v_rcp_f32_e32 v96, v96
	v_rcp_f32_e32 v97, v97
	v_rcp_f32_e32 v98, v98
	v_rcp_f32_e32 v99, v99
	s_nop 0
	v_mul_f32_e32 v32, v32, v108
	v_mul_f32_e32 v48, v48, v108
	v_mul_f32_e32 v64, v64, v108
	v_mul_f32_e32 v80, v80, v108
	v_mul_f32_e32 v33, v33, v109
	v_mul_f32_e32 v49, v49, v109
	v_mul_f32_e32 v65, v65, v109
	v_mul_f32_e32 v81, v81, v109
	v_mul_f32_e32 v34, v34, v110
	v_mul_f32_e32 v50, v50, v110
	v_mul_f32_e32 v66, v66, v110
	v_mul_f32_e32 v82, v82, v110
	v_mul_f32_e32 v35, v35, v111
	v_mul_f32_e32 v51, v51, v111
	v_mul_f32_e32 v67, v67, v111
	v_mul_f32_e32 v83, v83, v111
	v_mul_f32_e32 v36, v36, v104
	v_mul_f32_e32 v52, v52, v104
	v_mul_f32_e32 v68, v68, v104
	v_mul_f32_e32 v84, v84, v104
	v_mul_f32_e32 v37, v37, v105
	v_mul_f32_e32 v53, v53, v105
	v_mul_f32_e32 v69, v69, v105
	v_mul_f32_e32 v85, v85, v105
	v_mul_f32_e32 v38, v38, v106
	v_mul_f32_e32 v54, v54, v106
	v_mul_f32_e32 v70, v70, v106
	v_mul_f32_e32 v86, v86, v106
	v_mul_f32_e32 v39, v39, v107
	v_mul_f32_e32 v55, v55, v107
	v_mul_f32_e32 v71, v71, v107
	v_mul_f32_e32 v87, v87, v107
	v_mul_f32_e32 v40, v40, v100
	v_mul_f32_e32 v56, v56, v100
	v_mul_f32_e32 v72, v72, v100
	v_mul_f32_e32 v88, v88, v100
	v_mul_f32_e32 v41, v41, v101
	v_mul_f32_e32 v57, v57, v101
	v_mul_f32_e32 v73, v73, v101
	v_mul_f32_e32 v89, v89, v101
	v_mul_f32_e32 v42, v42, v102
	v_mul_f32_e32 v58, v58, v102
	v_mul_f32_e32 v74, v74, v102
	v_mul_f32_e32 v90, v90, v102
	v_mul_f32_e32 v43, v43, v103
	v_mul_f32_e32 v59, v59, v103
	v_mul_f32_e32 v75, v75, v103
	v_mul_f32_e32 v91, v91, v103
	v_mul_f32_e32 v44, v44, v96
	v_mul_f32_e32 v60, v60, v96
	v_mul_f32_e32 v76, v76, v96
	v_mul_f32_e32 v92, v92, v96
	v_mul_f32_e32 v45, v45, v97
	v_mul_f32_e32 v61, v61, v97
	v_mul_f32_e32 v77, v77, v97
	v_mul_f32_e32 v93, v93, v97
	v_mul_f32_e32 v46, v46, v98
	v_mul_f32_e32 v62, v62, v98
	v_mul_f32_e32 v78, v78, v98
	v_mul_f32_e32 v94, v94, v98
	v_mul_f32_e32 v47, v47, v99
	v_mul_f32_e32 v63, v63, v99
	v_mul_f32_e32 v79, v79, v99
	v_mul_f32_e32 v95, v95, v99
	v_mov_b32_dpp v116, v32 quad_perm:[1,0,3,2] row_mask:0xf bank_mask:0xf
	v_cvt_pk_bf16_f32 v32, v32, v116
	v_mov_b32_dpp v117, v48 quad_perm:[1,0,3,2] row_mask:0xf bank_mask:0xf
	v_cvt_pk_bf16_f32 v48, v48, v117
	v_mov_b32_dpp v116, v64 quad_perm:[1,0,3,2] row_mask:0xf bank_mask:0xf
	v_cvt_pk_bf16_f32 v64, v64, v116
	v_mov_b32_dpp v117, v80 quad_perm:[1,0,3,2] row_mask:0xf bank_mask:0xf
	v_cvt_pk_bf16_f32 v80, v80, v117
	v_mov_b32_dpp v116, v33 quad_perm:[1,0,3,2] row_mask:0xf bank_mask:0xf
	v_cvt_pk_bf16_f32 v33, v33, v116
	v_mov_b32_dpp v117, v49 quad_perm:[1,0,3,2] row_mask:0xf bank_mask:0xf
	v_cvt_pk_bf16_f32 v49, v49, v117
	v_mov_b32_dpp v116, v65 quad_perm:[1,0,3,2] row_mask:0xf bank_mask:0xf
	v_cvt_pk_bf16_f32 v65, v65, v116
	v_mov_b32_dpp v117, v81 quad_perm:[1,0,3,2] row_mask:0xf bank_mask:0xf
	v_cvt_pk_bf16_f32 v81, v81, v117
	v_mov_b32_dpp v116, v34 quad_perm:[1,0,3,2] row_mask:0xf bank_mask:0xf
	v_cvt_pk_bf16_f32 v34, v34, v116
	v_mov_b32_dpp v117, v50 quad_perm:[1,0,3,2] row_mask:0xf bank_mask:0xf
	v_cvt_pk_bf16_f32 v50, v50, v117
	v_mov_b32_dpp v116, v66 quad_perm:[1,0,3,2] row_mask:0xf bank_mask:0xf
	v_cvt_pk_bf16_f32 v66, v66, v116
	v_mov_b32_dpp v117, v82 quad_perm:[1,0,3,2] row_mask:0xf bank_mask:0xf
	v_cvt_pk_bf16_f32 v82, v82, v117
	v_mov_b32_dpp v116, v35 quad_perm:[1,0,3,2] row_mask:0xf bank_mask:0xf
	v_cvt_pk_bf16_f32 v35, v35, v116
	v_mov_b32_dpp v117, v51 quad_perm:[1,0,3,2] row_mask:0xf bank_mask:0xf
	v_cvt_pk_bf16_f32 v51, v51, v117
	v_mov_b32_dpp v116, v67 quad_perm:[1,0,3,2] row_mask:0xf bank_mask:0xf
	v_cvt_pk_bf16_f32 v67, v67, v116
	v_mov_b32_dpp v117, v83 quad_perm:[1,0,3,2] row_mask:0xf bank_mask:0xf
	v_cvt_pk_bf16_f32 v83, v83, v117
	v_mov_b32_dpp v116, v36 quad_perm:[1,0,3,2] row_mask:0xf bank_mask:0xf
	v_cvt_pk_bf16_f32 v36, v36, v116
	v_mov_b32_dpp v117, v52 quad_perm:[1,0,3,2] row_mask:0xf bank_mask:0xf
	v_cvt_pk_bf16_f32 v52, v52, v117
	v_mov_b32_dpp v116, v68 quad_perm:[1,0,3,2] row_mask:0xf bank_mask:0xf
	v_cvt_pk_bf16_f32 v68, v68, v116
	v_mov_b32_dpp v117, v84 quad_perm:[1,0,3,2] row_mask:0xf bank_mask:0xf
	v_cvt_pk_bf16_f32 v84, v84, v117
	v_mov_b32_dpp v116, v37 quad_perm:[1,0,3,2] row_mask:0xf bank_mask:0xf
	v_cvt_pk_bf16_f32 v37, v37, v116
	v_mov_b32_dpp v117, v53 quad_perm:[1,0,3,2] row_mask:0xf bank_mask:0xf
	v_cvt_pk_bf16_f32 v53, v53, v117
	v_mov_b32_dpp v116, v69 quad_perm:[1,0,3,2] row_mask:0xf bank_mask:0xf
	v_cvt_pk_bf16_f32 v69, v69, v116
	v_mov_b32_dpp v117, v85 quad_perm:[1,0,3,2] row_mask:0xf bank_mask:0xf
	v_cvt_pk_bf16_f32 v85, v85, v117
	v_mov_b32_dpp v116, v38 quad_perm:[1,0,3,2] row_mask:0xf bank_mask:0xf
	v_cvt_pk_bf16_f32 v38, v38, v116
	v_mov_b32_dpp v117, v54 quad_perm:[1,0,3,2] row_mask:0xf bank_mask:0xf
	v_cvt_pk_bf16_f32 v54, v54, v117
	v_mov_b32_dpp v116, v70 quad_perm:[1,0,3,2] row_mask:0xf bank_mask:0xf
	v_cvt_pk_bf16_f32 v70, v70, v116
	v_mov_b32_dpp v117, v86 quad_perm:[1,0,3,2] row_mask:0xf bank_mask:0xf
; __device__ __forceinline__ unsigned cvtpk(float lo, float hi) { unsigned r; asm volatile("v_cvt_pk_bf16_f32 %0, %1, %2" : "=v"(r) : "v"(lo), "v"(hi)); return r; }
; __device__ __forceinline__ void moba_unit(const UnitRef& u, char* lds, int* rowtab, int* cq, float* wscr, int* idx_slot, const int pend_idx, const int wid) {
;     ...
;         for (int r = 0; r < 16; ++r) { const int orc = (r & 3) + 8 * (r >> 2);
; #pragma unroll
;             for (int d0 = 0; d0 < 4; ++d0) { const float v = o[d0][r] * rli[r];
;                 const float vn = __shfl_xor(v, 1);
;                 if ((r32 & 1) == 0) *(unsigned*)((char*)u.O + (size_t)(orc * OPITCH + d0 * 32) * 2 + ooff) = cvtpk(v, vn); } }
	v_cvt_pk_bf16_f32 v86, v86, v117
	v_mov_b32_dpp v116, v39 quad_perm:[1,0,3,2] row_mask:0xf bank_mask:0xf
	v_cvt_pk_bf16_f32 v39, v39, v116
	v_mov_b32_dpp v117, v55 quad_perm:[1,0,3,2] row_mask:0xf bank_mask:0xf
	v_cvt_pk_bf16_f32 v55, v55, v117
	v_mov_b32_dpp v116, v71 quad_perm:[1,0,3,2] row_mask:0xf bank_mask:0xf
	v_cvt_pk_bf16_f32 v71, v71, v116
	v_mov_b32_dpp v117, v87 quad_perm:[1,0,3,2] row_mask:0xf bank_mask:0xf
	v_cvt_pk_bf16_f32 v87, v87, v117
	v_mov_b32_dpp v116, v40 quad_perm:[1,0,3,2] row_mask:0xf bank_mask:0xf
	v_cvt_pk_bf16_f32 v40, v40, v116
	v_mov_b32_dpp v117, v56 quad_perm:[1,0,3,2] row_mask:0xf bank_mask:0xf
	v_cvt_pk_bf16_f32 v56, v56, v117
	v_mov_b32_dpp v116, v72 quad_perm:[1,0,3,2] row_mask:0xf bank_mask:0xf
	v_cvt_pk_bf16_f32 v72, v72, v116
	v_mov_b32_dpp v117, v88 quad_perm:[1,0,3,2] row_mask:0xf bank_mask:0xf
	v_cvt_pk_bf16_f32 v88, v88, v117
	v_mov_b32_dpp v116, v41 quad_perm:[1,0,3,2] row_mask:0xf bank_mask:0xf
	v_cvt_pk_bf16_f32 v41, v41, v116
	v_mov_b32_dpp v117, v57 quad_perm:[1,0,3,2] row_mask:0xf bank_mask:0xf
	v_cvt_pk_bf16_f32 v57, v57, v117
	v_mov_b32_dpp v116, v73 quad_perm:[1,0,3,2] row_mask:0xf bank_mask:0xf
	v_cvt_pk_bf16_f32 v73, v73, v116
	v_mov_b32_dpp v117, v89 quad_perm:[1,0,3,2] row_mask:0xf bank_mask:0xf
	v_cvt_pk_bf16_f32 v89, v89, v117
	v_mov_b32_dpp v116, v42 quad_perm:[1,0,3,2] row_mask:0xf bank_mask:0xf
	v_cvt_pk_bf16_f32 v42, v42, v116
	v_mov_b32_dpp v117, v58 quad_perm:[1,0,3,2] row_mask:0xf bank_mask:0xf
	v_cvt_pk_bf16_f32 v58, v58, v117
	v_mov_b32_dpp v116, v74 quad_perm:[1,0,3,2] row_mask:0xf bank_mask:0xf
	v_cvt_pk_bf16_f32 v74, v74, v116
	v_mov_b32_dpp v117, v90 quad_perm:[1,0,3,2] row_mask:0xf bank_mask:0xf
	v_cvt_pk_bf16_f32 v90, v90, v117
	v_mov_b32_dpp v116, v43 quad_perm:[1,0,3,2] row_mask:0xf bank_mask:0xf
	v_cvt_pk_bf16_f32 v43, v43, v116
	v_mov_b32_dpp v117, v59 quad_perm:[1,0,3,2] row_mask:0xf bank_mask:0xf
	v_cvt_pk_bf16_f32 v59, v59, v117
	v_mov_b32_dpp v116, v75 quad_perm:[1,0,3,2] row_mask:0xf bank_mask:0xf
	v_cvt_pk_bf16_f32 v75, v75, v116
	v_mov_b32_dpp v117, v91 quad_perm:[1,0,3,2] row_mask:0xf bank_mask:0xf
	v_cvt_pk_bf16_f32 v91, v91, v117
	v_mov_b32_dpp v116, v44 quad_perm:[1,0,3,2] row_mask:0xf bank_mask:0xf
	v_cvt_pk_bf16_f32 v44, v44, v116
	v_mov_b32_dpp v117, v60 quad_perm:[1,0,3,2] row_mask:0xf bank_mask:0xf
	v_cvt_pk_bf16_f32 v60, v60, v117
	v_mov_b32_dpp v116, v76 quad_perm:[1,0,3,2] row_mask:0xf bank_mask:0xf
	v_cvt_pk_bf16_f32 v76, v76, v116
	v_mov_b32_dpp v117, v92 quad_perm:[1,0,3,2] row_mask:0xf bank_mask:0xf
	v_cvt_pk_bf16_f32 v92, v92, v117
	v_mov_b32_dpp v116, v45 quad_perm:[1,0,3,2] row_mask:0xf bank_mask:0xf
	v_cvt_pk_bf16_f32 v45, v45, v116
	v_mov_b32_dpp v117, v61 quad_perm:[1,0,3,2] row_mask:0xf bank_mask:0xf
	v_cvt_pk_bf16_f32 v61, v61, v117
	v_mov_b32_dpp v116, v77 quad_perm:[1,0,3,2] row_mask:0xf bank_mask:0xf
	v_cvt_pk_bf16_f32 v77, v77, v116
	v_mov_b32_dpp v117, v93 quad_perm:[1,0,3,2] row_mask:0xf bank_mask:0xf
	v_cvt_pk_bf16_f32 v93, v93, v117
	v_mov_b32_dpp v116, v46 quad_perm:[1,0,3,2] row_mask:0xf bank_mask:0xf
	v_cvt_pk_bf16_f32 v46, v46, v116
	v_mov_b32_dpp v117, v62 quad_perm:[1,0,3,2] row_mask:0xf bank_mask:0xf
	v_cvt_pk_bf16_f32 v62, v62, v117
	v_mov_b32_dpp v116, v78 quad_perm:[1,0,3,2] row_mask:0xf bank_mask:0xf
	v_cvt_pk_bf16_f32 v78, v78, v116
	v_mov_b32_dpp v117, v94 quad_perm:[1,0,3,2] row_mask:0xf bank_mask:0xf
	v_cvt_pk_bf16_f32 v94, v94, v117
	v_mov_b32_dpp v116, v47 quad_perm:[1,0,3,2] row_mask:0xf bank_mask:0xf
	v_cvt_pk_bf16_f32 v47, v47, v116
	v_mov_b32_dpp v117, v63 quad_perm:[1,0,3,2] row_mask:0xf bank_mask:0xf
; __device__ __forceinline__ unsigned cvtpk(float lo, float hi) { unsigned r; asm volatile("v_cvt_pk_bf16_f32 %0, %1, %2" : "=v"(r) : "v"(lo), "v"(hi)); return r; }
; __device__ __forceinline__ void moba_unit(const UnitRef& u, char* lds, int* rowtab, int* cq, float* wscr, int* idx_slot, const int pend_idx, const int wid) {
;     ...
;         for (int r = 0; r < 16; ++r) { const int orc = (r & 3) + 8 * (r >> 2);
; #pragma unroll
;             for (int d0 = 0; d0 < 4; ++d0) { const float v = o[d0][r] * rli[r];
;                 const float vn = __shfl_xor(v, 1);
;                 if ((r32 & 1) == 0) *(unsigned*)((char*)u.O + (size_t)(orc * OPITCH + d0 * 32) * 2 + ooff) = cvtpk(v, vn); } }
	v_cvt_pk_bf16_f32 v63, v63, v117
	v_mov_b32_dpp v116, v79 quad_perm:[1,0,3,2] row_mask:0xf bank_mask:0xf
	v_cvt_pk_bf16_f32 v79, v79, v116
	v_mov_b32_dpp v117, v95 quad_perm:[1,0,3,2] row_mask:0xf bank_mask:0xf
	v_cvt_pk_bf16_f32 v95, v95, v117
	s_and_saveexec_b64 s[10:11], s[6:7]
	global_store_dword v[114:115], v32, off
	global_store_dword v[114:115], v48, off offset:64
	global_store_dword v[114:115], v64, off offset:128
	global_store_dword v[114:115], v80, off offset:192
	global_store_dword v[114:115], v33, off offset:256
	global_store_dword v[114:115], v49, off offset:320
	global_store_dword v[114:115], v65, off offset:384
	global_store_dword v[114:115], v81, off offset:448
	global_store_dword v[114:115], v34, off offset:512
	global_store_dword v[114:115], v50, off offset:576
	global_store_dword v[114:115], v66, off offset:640
	global_store_dword v[114:115], v82, off offset:704
	global_store_dword v[114:115], v35, off offset:768
	global_store_dword v[114:115], v51, off offset:832
	global_store_dword v[114:115], v67, off offset:896
	global_store_dword v[114:115], v83, off offset:960
	global_store_dword v[114:115], v36, off offset:2048
	global_store_dword v[114:115], v52, off offset:2112
	global_store_dword v[114:115], v68, off offset:2176
	global_store_dword v[114:115], v84, off offset:2240
	global_store_dword v[114:115], v37, off offset:2304
	global_store_dword v[114:115], v53, off offset:2368
	global_store_dword v[114:115], v69, off offset:2432
	global_store_dword v[114:115], v85, off offset:2496
	global_store_dword v[114:115], v38, off offset:2560
	global_store_dword v[114:115], v54, off offset:2624
	global_store_dword v[114:115], v70, off offset:2688
	global_store_dword v[114:115], v86, off offset:2752
	global_store_dword v[114:115], v39, off offset:2816
	global_store_dword v[114:115], v55, off offset:2880
	global_store_dword v[114:115], v71, off offset:2944
	global_store_dword v[114:115], v87, off offset:3008
	global_store_dword v[118:119], v40, off
	global_store_dword v[118:119], v56, off offset:64
	global_store_dword v[118:119], v72, off offset:128
	global_store_dword v[118:119], v88, off offset:192
	global_store_dword v[118:119], v41, off offset:256
	global_store_dword v[118:119], v57, off offset:320
	global_store_dword v[118:119], v73, off offset:384
	global_store_dword v[118:119], v89, off offset:448
	global_store_dword v[118:119], v42, off offset:512
	global_store_dword v[118:119], v58, off offset:576
	global_store_dword v[118:119], v74, off offset:640
	global_store_dword v[118:119], v90, off offset:704
	global_store_dword v[118:119], v43, off offset:768
	global_store_dword v[118:119], v59, off offset:832
	global_store_dword v[118:119], v75, off offset:896
	global_store_dword v[118:119], v91, off offset:960
	global_store_dword v[118:119], v44, off offset:2048
	global_store_dword v[118:119], v60, off offset:2112
	global_store_dword v[118:119], v76, off offset:2176
	global_store_dword v[118:119], v92, off offset:2240
	global_store_dword v[118:119], v45, off offset:2304
	global_store_dword v[118:119], v61, off offset:2368
	global_store_dword v[118:119], v77, off offset:2432
	global_store_dword v[118:119], v93, off offset:2496
	global_store_dword v[118:119], v46, off offset:2560
	global_store_dword v[118:119], v62, off offset:2624
	global_store_dword v[118:119], v78, off offset:2688
	global_store_dword v[118:119], v94, off offset:2752
	global_store_dword v[118:119], v47, off offset:2816
	global_store_dword v[118:119], v63, off offset:2880
	global_store_dword v[118:119], v79, off offset:2944
	global_store_dword v[118:119], v95, off offset:3008
